# GQA fast loop without K prefetch; wave halves run QK^T(j+1) and finish-softmax(j) in opposite order (role swap)
# speedup vs baseline: 1.0056x; 1.0056x over previous
.LBB0_881:
	v_readlane_b32 s2, v251, 4
	s_nop 3
	s_cmp_lt_u32 s2, 4
	s_cbranch_scc1 .Lgqa_B_fq
	ds_read_b128 v[96:99], v216 offset:49152
	ds_read_b128 v[100:103], v216 offset:57344
	ds_read_b128 v[178:181], v218 offset:49152
	ds_read_b128 v[182:185], v218 offset:57344
	s_waitcnt lgkmcnt(3)
	v_mfma_f32_32x32x16_bf16 v[112:127], v[96:99], v[138:141], 0
	s_waitcnt lgkmcnt(2)
	v_mfma_f32_32x32x16_bf16 v[96:111], v[100:103], v[138:141], 0
	s_waitcnt lgkmcnt(1)
	v_mfma_f32_32x32x16_bf16 v[112:127], v[178:181], v[154:157], v[112:127]
	s_waitcnt lgkmcnt(0)
	v_mfma_f32_32x32x16_bf16 v[96:111], v[182:185], v[154:157], v[96:111]
	ds_read_b128 v[178:181], v219 offset:49152
	ds_read_b128 v[182:185], v219 offset:57344
	s_waitcnt lgkmcnt(1)
	v_mfma_f32_32x32x16_bf16 v[112:127], v[178:181], v[158:161], v[112:127]
	s_waitcnt lgkmcnt(0)
	v_mfma_f32_32x32x16_bf16 v[96:111], v[182:185], v[158:161], v[96:111]
	ds_read_b128 v[178:181], v220 offset:49152
	ds_read_b128 v[182:185], v220 offset:57344
	s_waitcnt lgkmcnt(1)
	v_mfma_f32_32x32x16_bf16 v[112:127], v[178:181], v[150:153], v[112:127]
	s_waitcnt lgkmcnt(0)
	v_mfma_f32_32x32x16_bf16 v[96:111], v[182:185], v[150:153], v[96:111]
	ds_read_b128 v[178:181], v221 offset:49152
	ds_read_b128 v[182:185], v221 offset:57344
	s_waitcnt lgkmcnt(1)
	v_mfma_f32_32x32x16_bf16 v[112:127], v[178:181], v[146:149], v[112:127]
	s_waitcnt lgkmcnt(0)
	v_mfma_f32_32x32x16_bf16 v[96:111], v[182:185], v[146:149], v[96:111]
	ds_read_b128 v[178:181], v222 offset:49152
	ds_read_b128 v[182:185], v222 offset:57344
	s_waitcnt lgkmcnt(1)
	v_mfma_f32_32x32x16_bf16 v[112:127], v[178:181], v[142:145], v[112:127]
	s_waitcnt lgkmcnt(0)
	v_mfma_f32_32x32x16_bf16 v[96:111], v[182:185], v[142:145], v[96:111]
	ds_read_b128 v[178:181], v224 offset:49152
	ds_read_b128 v[182:185], v224 offset:57344
	s_waitcnt lgkmcnt(1)
	v_mfma_f32_32x32x16_bf16 v[112:127], v[178:181], v[134:137], v[112:127]
	s_waitcnt lgkmcnt(0)
	v_mfma_f32_32x32x16_bf16 v[96:111], v[182:185], v[134:137], v[96:111]
	ds_read_b128 v[178:181], v223 offset:49152
	ds_read_b128 v[182:185], v223 offset:57344
	s_waitcnt lgkmcnt(1)
	v_mfma_f32_32x32x16_bf16 v[112:127], v[178:181], v[130:133], v[112:127]
	s_waitcnt lgkmcnt(0)
	v_mfma_f32_32x32x16_bf16 v[96:111], v[182:185], v[130:133], v[96:111]
	v_add_f32_e32 v88, v64, v65
	v_add_f32_e32 v89, v72, v73
	v_add_f32_e32 v90, v80, v81
	v_add_f32_e32 v91, v194, v195
	v_add_f32_e32 v88, v66, v88
	v_add_f32_e32 v89, v74, v89
	v_add_f32_e32 v90, v82, v90
	v_add_f32_e32 v91, v196, v91
	v_add_f32_e32 v88, v67, v88
	v_add_f32_e32 v89, v75, v89
	v_add_f32_e32 v90, v83, v90
	v_add_f32_e32 v91, v197, v91
	v_add_f32_e32 v88, v68, v88
	v_add_f32_e32 v89, v76, v89
	v_add_f32_e32 v90, v84, v90
	v_add_f32_e32 v91, v92, v91
	v_add_f32_e32 v88, v69, v88
	v_add_f32_e32 v89, v77, v89
	v_add_f32_e32 v90, v85, v90
	v_add_f32_e32 v91, v93, v91
	v_add_f32_e32 v88, v70, v88
	v_add_f32_e32 v89, v78, v89
	v_add_f32_e32 v90, v86, v90
	v_add_f32_e32 v91, v94, v91
	v_add_f32_e32 v88, v71, v88
	v_add_f32_e32 v89, v79, v89
	v_add_f32_e32 v90, v87, v90
	v_add_f32_e32 v91, v95, v91
	v_add_f32_e32 v88, v89, v88
	v_add_f32_e32 v89, v91, v90
	v_add_f32_e32 v227, v88, v89
	v_mov_b32_e32 v228, v227
	v_cvt_pk_bf16_f32 v88, v64, v65
	v_cvt_pk_bf16_f32 v89, v66, v67
	v_cvt_pk_bf16_f32 v90, v68, v69
	v_cvt_pk_bf16_f32 v91, v70, v71
	v_permlane32_swap_b32_e32 v227, v228
	v_permlane32_swap_b32_e32 v88, v90
	v_permlane32_swap_b32_e32 v89, v91
	v_cvt_pk_bf16_f32 v72, v72, v73
	v_cvt_pk_bf16_f32 v73, v74, v75
	v_cvt_pk_bf16_f32 v74, v76, v77
	v_cvt_pk_bf16_f32 v75, v78, v79
	v_cvt_pk_bf16_f32 v64, v80, v81
	v_cvt_pk_bf16_f32 v65, v82, v83
	v_cvt_pk_bf16_f32 v66, v84, v85
	v_cvt_pk_bf16_f32 v67, v86, v87
	v_cvt_pk_bf16_f32 v68, v194, v195
	v_cvt_pk_bf16_f32 v69, v196, v197
	v_cvt_pk_bf16_f32 v70, v92, v93
	v_cvt_pk_bf16_f32 v71, v94, v95
	v_permlane32_swap_b32_e32 v72, v74
	v_permlane32_swap_b32_e32 v73, v75
	v_permlane32_swap_b32_e32 v64, v66
	v_permlane32_swap_b32_e32 v65, v67
	v_permlane32_swap_b32_e32 v68, v70
	v_permlane32_swap_b32_e32 v69, v71
	s_branch .Lgqa_B_join
.Lgqa_B_fq:
	v_add_f32_e32 v88, v64, v65
	v_add_f32_e32 v89, v72, v73
	v_add_f32_e32 v90, v80, v81
	v_add_f32_e32 v91, v194, v195
	v_add_f32_e32 v88, v66, v88
	v_add_f32_e32 v89, v74, v89
	v_add_f32_e32 v90, v82, v90
	v_add_f32_e32 v91, v196, v91
	v_add_f32_e32 v88, v67, v88
	v_add_f32_e32 v89, v75, v89
	v_add_f32_e32 v90, v83, v90
	v_add_f32_e32 v91, v197, v91
	v_add_f32_e32 v88, v68, v88
	v_add_f32_e32 v89, v76, v89
	v_add_f32_e32 v90, v84, v90
	v_add_f32_e32 v91, v92, v91
	v_add_f32_e32 v88, v69, v88
	v_add_f32_e32 v89, v77, v89
	v_add_f32_e32 v90, v85, v90
	v_add_f32_e32 v91, v93, v91
	v_add_f32_e32 v88, v70, v88
	v_add_f32_e32 v89, v78, v89
	v_add_f32_e32 v90, v86, v90
	v_add_f32_e32 v91, v94, v91
	v_add_f32_e32 v88, v71, v88
	v_add_f32_e32 v89, v79, v89
	v_add_f32_e32 v90, v87, v90
	v_add_f32_e32 v91, v95, v91
	v_add_f32_e32 v88, v89, v88
	v_add_f32_e32 v89, v91, v90
	v_add_f32_e32 v227, v88, v89
	v_mov_b32_e32 v228, v227
	v_cvt_pk_bf16_f32 v88, v64, v65
	v_cvt_pk_bf16_f32 v89, v66, v67
	v_cvt_pk_bf16_f32 v90, v68, v69
	v_cvt_pk_bf16_f32 v91, v70, v71
	v_permlane32_swap_b32_e32 v227, v228
	v_permlane32_swap_b32_e32 v88, v90
	v_permlane32_swap_b32_e32 v89, v91
	v_cvt_pk_bf16_f32 v72, v72, v73
	v_cvt_pk_bf16_f32 v73, v74, v75
	v_cvt_pk_bf16_f32 v74, v76, v77
	v_cvt_pk_bf16_f32 v75, v78, v79
	v_cvt_pk_bf16_f32 v64, v80, v81
	v_cvt_pk_bf16_f32 v65, v82, v83
	v_cvt_pk_bf16_f32 v66, v84, v85
	v_cvt_pk_bf16_f32 v67, v86, v87
	v_cvt_pk_bf16_f32 v68, v194, v195
	v_cvt_pk_bf16_f32 v69, v196, v197
	v_cvt_pk_bf16_f32 v70, v92, v93
	v_cvt_pk_bf16_f32 v71, v94, v95
	v_permlane32_swap_b32_e32 v72, v74
	v_permlane32_swap_b32_e32 v73, v75
	v_permlane32_swap_b32_e32 v64, v66
	v_permlane32_swap_b32_e32 v65, v67
	v_permlane32_swap_b32_e32 v68, v70
	v_permlane32_swap_b32_e32 v69, v71
	ds_read_b128 v[96:99], v216 offset:49152
	ds_read_b128 v[100:103], v216 offset:57344
	ds_read_b128 v[178:181], v218 offset:49152
	ds_read_b128 v[182:185], v218 offset:57344
	s_waitcnt lgkmcnt(3)
	v_mfma_f32_32x32x16_bf16 v[112:127], v[96:99], v[138:141], 0
	s_waitcnt lgkmcnt(2)
	v_mfma_f32_32x32x16_bf16 v[96:111], v[100:103], v[138:141], 0
	s_waitcnt lgkmcnt(1)
	v_mfma_f32_32x32x16_bf16 v[112:127], v[178:181], v[154:157], v[112:127]
	s_waitcnt lgkmcnt(0)
	v_mfma_f32_32x32x16_bf16 v[96:111], v[182:185], v[154:157], v[96:111]
	ds_read_b128 v[178:181], v219 offset:49152
	ds_read_b128 v[182:185], v219 offset:57344
	s_waitcnt lgkmcnt(1)
	v_mfma_f32_32x32x16_bf16 v[112:127], v[178:181], v[158:161], v[112:127]
	s_waitcnt lgkmcnt(0)
	v_mfma_f32_32x32x16_bf16 v[96:111], v[182:185], v[158:161], v[96:111]
	ds_read_b128 v[178:181], v220 offset:49152
	ds_read_b128 v[182:185], v220 offset:57344
	s_waitcnt lgkmcnt(1)
	v_mfma_f32_32x32x16_bf16 v[112:127], v[178:181], v[150:153], v[112:127]
	s_waitcnt lgkmcnt(0)
	v_mfma_f32_32x32x16_bf16 v[96:111], v[182:185], v[150:153], v[96:111]
	ds_read_b128 v[178:181], v221 offset:49152
	ds_read_b128 v[182:185], v221 offset:57344
	s_waitcnt lgkmcnt(1)
	v_mfma_f32_32x32x16_bf16 v[112:127], v[178:181], v[146:149], v[112:127]
	s_waitcnt lgkmcnt(0)
	v_mfma_f32_32x32x16_bf16 v[96:111], v[182:185], v[146:149], v[96:111]
	ds_read_b128 v[178:181], v222 offset:49152
	ds_read_b128 v[182:185], v222 offset:57344
	s_waitcnt lgkmcnt(1)
	v_mfma_f32_32x32x16_bf16 v[112:127], v[178:181], v[142:145], v[112:127]
	s_waitcnt lgkmcnt(0)
	v_mfma_f32_32x32x16_bf16 v[96:111], v[182:185], v[142:145], v[96:111]
	ds_read_b128 v[178:181], v224 offset:49152
	ds_read_b128 v[182:185], v224 offset:57344
	s_waitcnt lgkmcnt(1)
	v_mfma_f32_32x32x16_bf16 v[112:127], v[178:181], v[134:137], v[112:127]
	s_waitcnt lgkmcnt(0)
	v_mfma_f32_32x32x16_bf16 v[96:111], v[182:185], v[134:137], v[96:111]
	ds_read_b128 v[178:181], v223 offset:49152
	ds_read_b128 v[182:185], v223 offset:57344
	s_waitcnt lgkmcnt(1)
	v_mfma_f32_32x32x16_bf16 v[112:127], v[178:181], v[130:133], v[112:127]
	s_waitcnt lgkmcnt(0)
	v_mfma_f32_32x32x16_bf16 v[96:111], v[182:185], v[130:133], v[96:111]
.Lgqa_B_join:
	s_add_i32 s2, s39, -1
	s_mul_i32 s2, s2, s62
	s_lshl_b32 s72, s2, 6
	s_lshl_b64 s[2:3], s[72:73], 1
	s_add_u32 s12, s10, s2
	s_addc_u32 s13, s11, s3
	s_add_u32 s2, s8, s2
	s_addc_u32 s3, s9, s3
	global_load_dwordx4 v[178:181], v128, s[12:13]
	global_load_dwordx4 v[182:185], v198, s[12:13]
	global_load_dwordx4 v[186:189], v128, s[2:3]
	global_load_dwordx4 v[190:193], v198, s[2:3]
	ds_read_b64_tr_b16 v[76:77], v209 offset:0
	ds_read_b64_tr_b16 v[78:79], v209 offset:0x800
	ds_read_b64_tr_b16 v[80:81], v209 offset:0x1000
	ds_read_b64_tr_b16 v[82:83], v209 offset:0x1800
	ds_read_b64_tr_b16 v[84:85], v209 offset:0x2000
	ds_read_b64_tr_b16 v[86:87], v209 offset:0x2800
	ds_read_b64_tr_b16 v[92:93], v209 offset:0x3000
	ds_read_b64_tr_b16 v[94:95], v209 offset:0x3800
	s_waitcnt lgkmcnt(0)
	s_nop 0
	v_mfma_f32_32x32x16_bf16 v[0:15], v[76:79], v[88:91], v[0:15]
	v_mfma_f32_32x32x16_bf16 v[0:15], v[80:83], v[72:75], v[0:15]
	v_mfma_f32_32x32x16_bf16 v[0:15], v[84:87], v[64:67], v[0:15]
	ds_read_b64_tr_b16 v[76:77], v209 offset:0x200
	ds_read_b64_tr_b16 v[78:79], v209 offset:0xa00
	ds_read_b64_tr_b16 v[80:81], v209 offset:0x1200
	v_mfma_f32_32x32x16_bf16 v[0:15], v[92:95], v[68:71], v[0:15]
	ds_read_b64_tr_b16 v[82:83], v209 offset:0x1a00
	ds_read_b64_tr_b16 v[84:85], v209 offset:0x2200
	ds_read_b64_tr_b16 v[86:87], v209 offset:0x2a00
	ds_read_b64_tr_b16 v[92:93], v209 offset:0x3200
	ds_read_b64_tr_b16 v[94:95], v209 offset:0x3a00
	s_waitcnt lgkmcnt(0)
	v_mfma_f32_32x32x16_bf16 v[48:63], v[76:79], v[88:91], v[48:63]
	v_mfma_f32_32x32x16_bf16 v[48:63], v[80:83], v[72:75], v[48:63]
	v_mfma_f32_32x32x16_bf16 v[48:63], v[84:87], v[64:67], v[48:63]
	ds_read_b64_tr_b16 v[76:77], v209 offset:0x400
	ds_read_b64_tr_b16 v[78:79], v209 offset:0xc00
	ds_read_b64_tr_b16 v[80:81], v209 offset:0x1400
	ds_read_b64_tr_b16 v[82:83], v209 offset:0x1c00
	v_mfma_f32_32x32x16_bf16 v[48:63], v[92:95], v[68:71], v[48:63]
	ds_read_b64_tr_b16 v[84:85], v209 offset:0x2400
	ds_read_b64_tr_b16 v[86:87], v209 offset:0x2c00
	ds_read_b64_tr_b16 v[92:93], v209 offset:0x3400
	ds_read_b64_tr_b16 v[94:95], v209 offset:0x3c00
	s_waitcnt lgkmcnt(0)
	v_mfma_f32_32x32x16_bf16 v[32:47], v[76:79], v[88:91], v[32:47]
	ds_read_b64_tr_b16 v[76:77], v209 offset:0x600
	ds_read_b64_tr_b16 v[78:79], v209 offset:0xe00
	v_exp_f32_e32 v234, v104
	v_exp_f32_e32 v235, v105
	v_exp_f32_e32 v236, v106
	v_exp_f32_e32 v237, v107
	v_exp_f32_e32 v238, v108
	v_exp_f32_e32 v239, v109
	v_exp_f32_e32 v240, v110
	v_exp_f32_e32 v241, v111
	v_mfma_f32_32x32x16_bf16 v[32:47], v[80:83], v[72:75], v[32:47]
	v_exp_f32_e32 v80, v112
	v_exp_f32_e32 v81, v113
	v_exp_f32_e32 v82, v114
	v_exp_f32_e32 v83, v115
	v_mfma_f32_32x32x16_bf16 v[32:47], v[84:87], v[64:67], v[32:47]
	v_exp_f32_e32 v84, v116
	v_exp_f32_e32 v85, v117
	v_exp_f32_e32 v86, v118
	v_exp_f32_e32 v87, v119
	v_exp_f32_e32 v112, v96
	v_exp_f32_e32 v113, v97
	v_exp_f32_e32 v114, v98
	v_exp_f32_e32 v115, v99
	v_exp_f32_e32 v116, v100
	v_exp_f32_e32 v117, v101
	v_exp_f32_e32 v118, v102
	v_exp_f32_e32 v119, v103
	v_mfma_f32_32x32x16_bf16 v[32:47], v[92:95], v[68:71], v[32:47]
	ds_read_b64_tr_b16 v[92:93], v209 offset:0x1600
	ds_read_b64_tr_b16 v[94:95], v209 offset:0x1e00
	ds_read_b64_tr_b16 v[96:97], v209 offset:0x2600
	ds_read_b64_tr_b16 v[98:99], v209 offset:0x2e00
	ds_read_b64_tr_b16 v[100:101], v209 offset:0x3600
	ds_read_b64_tr_b16 v[102:103], v209 offset:0x3e00
	s_waitcnt lgkmcnt(0)
	v_mfma_f32_32x32x16_bf16 v[16:31], v[76:79], v[88:91], v[16:31]
	v_exp_f32_e32 v88, v120
	v_exp_f32_e32 v89, v121
	v_exp_f32_e32 v90, v122
	v_exp_f32_e32 v91, v123
	v_mfma_f32_32x32x16_bf16 v[16:31], v[92:95], v[72:75], v[16:31]
	v_exp_f32_e32 v92, v124
	v_exp_f32_e32 v93, v125
	v_exp_f32_e32 v94, v126
	v_exp_f32_e32 v95, v127
	s_barrier
	v_mfma_f32_32x32x16_bf16 v[16:31], v[96:99], v[64:67], v[16:31]
	s_waitcnt vmcnt(4)
	s_waitcnt vmcnt(7)
	ds_write_b128 v212, v[162:165]
	s_waitcnt vmcnt(6)
	ds_write_b128 v213, v[166:169]
	s_waitcnt vmcnt(5)
	ds_write_b128 v214, v[170:173] offset:32768
	s_waitcnt vmcnt(4)
	ds_write_b128 v215, v[174:177] offset:32768
	v_mfma_f32_32x32x16_bf16 v[16:31], v[100:103], v[68:71], v[16:31]
.LBB0_883:
	s_waitcnt lgkmcnt(0)
	s_barrier
	v_readlane_b32 s2, v251, 4
	s_nop 3
	s_cmp_lt_u32 s2, 4
	s_cbranch_scc1 .Lgqa_A_fq
	ds_read_b128 v[64:67], v216 offset:32768
	ds_read_b128 v[68:71], v216 offset:40960
	ds_read_b128 v[162:165], v218 offset:32768
	ds_read_b128 v[166:169], v218 offset:40960
	s_waitcnt lgkmcnt(3)
	v_mfma_f32_32x32x16_bf16 v[96:111], v[64:67], v[138:141], 0
	s_waitcnt lgkmcnt(2)
	v_mfma_f32_32x32x16_bf16 v[64:79], v[68:71], v[138:141], 0
	s_waitcnt lgkmcnt(1)
	v_mfma_f32_32x32x16_bf16 v[96:111], v[162:165], v[154:157], v[96:111]
	s_waitcnt lgkmcnt(0)
	v_mfma_f32_32x32x16_bf16 v[64:79], v[166:169], v[154:157], v[64:79]
	ds_read_b128 v[162:165], v219 offset:32768
	ds_read_b128 v[166:169], v219 offset:40960
	s_waitcnt lgkmcnt(1)
	v_mfma_f32_32x32x16_bf16 v[96:111], v[162:165], v[158:161], v[96:111]
	s_waitcnt lgkmcnt(0)
	v_mfma_f32_32x32x16_bf16 v[64:79], v[166:169], v[158:161], v[64:79]
	ds_read_b128 v[162:165], v220 offset:32768
	ds_read_b128 v[166:169], v220 offset:40960
	s_waitcnt lgkmcnt(1)
	v_mfma_f32_32x32x16_bf16 v[96:111], v[162:165], v[150:153], v[96:111]
	s_waitcnt lgkmcnt(0)
	v_mfma_f32_32x32x16_bf16 v[64:79], v[166:169], v[150:153], v[64:79]
	ds_read_b128 v[162:165], v221 offset:32768
	ds_read_b128 v[166:169], v221 offset:40960
	s_waitcnt lgkmcnt(1)
	v_mfma_f32_32x32x16_bf16 v[96:111], v[162:165], v[146:149], v[96:111]
	s_waitcnt lgkmcnt(0)
	v_mfma_f32_32x32x16_bf16 v[64:79], v[166:169], v[146:149], v[64:79]
	ds_read_b128 v[162:165], v222 offset:32768
	ds_read_b128 v[166:169], v222 offset:40960
	s_waitcnt lgkmcnt(1)
	v_mfma_f32_32x32x16_bf16 v[96:111], v[162:165], v[142:145], v[96:111]
	s_waitcnt lgkmcnt(0)
	v_mfma_f32_32x32x16_bf16 v[64:79], v[166:169], v[142:145], v[64:79]
	ds_read_b128 v[162:165], v224 offset:32768
	ds_read_b128 v[166:169], v224 offset:40960
	s_waitcnt lgkmcnt(1)
	v_mfma_f32_32x32x16_bf16 v[96:111], v[162:165], v[134:137], v[96:111]
	s_waitcnt lgkmcnt(0)
	v_mfma_f32_32x32x16_bf16 v[64:79], v[166:169], v[134:137], v[64:79]
	ds_read_b128 v[162:165], v223 offset:32768
	ds_read_b128 v[166:169], v223 offset:40960
	s_waitcnt lgkmcnt(1)
	v_mfma_f32_32x32x16_bf16 v[96:111], v[162:165], v[130:133], v[96:111]
	s_waitcnt lgkmcnt(0)
	v_mfma_f32_32x32x16_bf16 v[64:79], v[166:169], v[130:133], v[64:79]
	v_add_f32_e32 v120, v80, v81
	v_add_f32_e32 v121, v88, v89
	v_add_f32_e32 v122, v112, v113
	v_add_f32_e32 v123, v234, v235
	v_add_f32_e32 v120, v82, v120
	v_add_f32_e32 v121, v90, v121
	v_add_f32_e32 v122, v114, v122
	v_add_f32_e32 v123, v236, v123
	v_add_f32_e32 v120, v83, v120
	v_add_f32_e32 v121, v91, v121
	v_add_f32_e32 v122, v115, v122
	v_add_f32_e32 v123, v237, v123
	v_add_f32_e32 v120, v84, v120
	v_add_f32_e32 v121, v92, v121
	v_add_f32_e32 v122, v116, v122
	v_add_f32_e32 v123, v238, v123
	v_add_f32_e32 v120, v85, v120
	v_add_f32_e32 v121, v93, v121
	v_add_f32_e32 v122, v117, v122
	v_add_f32_e32 v123, v239, v123
	v_add_f32_e32 v120, v86, v120
	v_add_f32_e32 v121, v94, v121
	v_add_f32_e32 v122, v118, v122
	v_add_f32_e32 v123, v240, v123
	v_add_f32_e32 v120, v87, v120
	v_add_f32_e32 v121, v95, v121
	v_add_f32_e32 v122, v119, v122
	v_add_f32_e32 v123, v241, v123
	v_add_f32_e32 v120, v121, v120
	v_add_f32_e32 v121, v123, v122
	v_add_f32_e32 v229, v120, v121
	v_mov_b32_e32 v233, v229
	s_nop 1
	v_permlane32_swap_b32_e32 v229, v233
	v_cvt_pk_bf16_f32 v124, v80, v81
	v_cvt_pk_bf16_f32 v125, v82, v83
	v_cvt_pk_bf16_f32 v126, v84, v85
	v_cvt_pk_bf16_f32 v127, v86, v87
	v_cvt_pk_bf16_f32 v120, v88, v89
	v_cvt_pk_bf16_f32 v121, v90, v91
	v_cvt_pk_bf16_f32 v122, v92, v93
	v_cvt_pk_bf16_f32 v123, v94, v95
	v_cvt_pk_bf16_f32 v112, v112, v113
	v_cvt_pk_bf16_f32 v113, v114, v115
	v_cvt_pk_bf16_f32 v114, v116, v117
	v_cvt_pk_bf16_f32 v115, v118, v119
	v_cvt_pk_bf16_f32 v116, v234, v235
	v_cvt_pk_bf16_f32 v117, v236, v237
	v_cvt_pk_bf16_f32 v118, v238, v239
	v_cvt_pk_bf16_f32 v119, v240, v241
	v_permlane32_swap_b32_e32 v124, v126
	v_permlane32_swap_b32_e32 v125, v127
	v_permlane32_swap_b32_e32 v120, v122
	v_permlane32_swap_b32_e32 v121, v123
	v_permlane32_swap_b32_e32 v112, v114
	v_permlane32_swap_b32_e32 v113, v115
	v_permlane32_swap_b32_e32 v116, v118
	v_permlane32_swap_b32_e32 v117, v119
	s_branch .Lgqa_A_join
.Lgqa_A_fq:
	v_add_f32_e32 v120, v80, v81
	v_add_f32_e32 v121, v88, v89
	v_add_f32_e32 v122, v112, v113
	v_add_f32_e32 v123, v234, v235
	v_add_f32_e32 v120, v82, v120
	v_add_f32_e32 v121, v90, v121
	v_add_f32_e32 v122, v114, v122
	v_add_f32_e32 v123, v236, v123
	v_add_f32_e32 v120, v83, v120
	v_add_f32_e32 v121, v91, v121
	v_add_f32_e32 v122, v115, v122
	v_add_f32_e32 v123, v237, v123
	v_add_f32_e32 v120, v84, v120
	v_add_f32_e32 v121, v92, v121
	v_add_f32_e32 v122, v116, v122
	v_add_f32_e32 v123, v238, v123
	v_add_f32_e32 v120, v85, v120
	v_add_f32_e32 v121, v93, v121
	v_add_f32_e32 v122, v117, v122
	v_add_f32_e32 v123, v239, v123
	v_add_f32_e32 v120, v86, v120
	v_add_f32_e32 v121, v94, v121
	v_add_f32_e32 v122, v118, v122
	v_add_f32_e32 v123, v240, v123
	v_add_f32_e32 v120, v87, v120
	v_add_f32_e32 v121, v95, v121
	v_add_f32_e32 v122, v119, v122
	v_add_f32_e32 v123, v241, v123
	v_add_f32_e32 v120, v121, v120
	v_add_f32_e32 v121, v123, v122
	v_add_f32_e32 v229, v120, v121
	v_mov_b32_e32 v233, v229
	s_nop 1
	v_permlane32_swap_b32_e32 v229, v233
	v_cvt_pk_bf16_f32 v124, v80, v81
	v_cvt_pk_bf16_f32 v125, v82, v83
	v_cvt_pk_bf16_f32 v126, v84, v85
	v_cvt_pk_bf16_f32 v127, v86, v87
	v_cvt_pk_bf16_f32 v120, v88, v89
	v_cvt_pk_bf16_f32 v121, v90, v91
	v_cvt_pk_bf16_f32 v122, v92, v93
	v_cvt_pk_bf16_f32 v123, v94, v95
	v_cvt_pk_bf16_f32 v112, v112, v113
	v_cvt_pk_bf16_f32 v113, v114, v115
	v_cvt_pk_bf16_f32 v114, v116, v117
	v_cvt_pk_bf16_f32 v115, v118, v119
	v_cvt_pk_bf16_f32 v116, v234, v235
	v_cvt_pk_bf16_f32 v117, v236, v237
	v_cvt_pk_bf16_f32 v118, v238, v239
	v_cvt_pk_bf16_f32 v119, v240, v241
	v_permlane32_swap_b32_e32 v124, v126
	v_permlane32_swap_b32_e32 v125, v127
	v_permlane32_swap_b32_e32 v120, v122
	v_permlane32_swap_b32_e32 v121, v123
	v_permlane32_swap_b32_e32 v112, v114
	v_permlane32_swap_b32_e32 v113, v115
	v_permlane32_swap_b32_e32 v116, v118
	v_permlane32_swap_b32_e32 v117, v119
	ds_read_b128 v[64:67], v216 offset:32768
	ds_read_b128 v[68:71], v216 offset:40960
	ds_read_b128 v[162:165], v218 offset:32768
	ds_read_b128 v[166:169], v218 offset:40960
	s_waitcnt lgkmcnt(3)
	v_mfma_f32_32x32x16_bf16 v[96:111], v[64:67], v[138:141], 0
	s_waitcnt lgkmcnt(2)
	v_mfma_f32_32x32x16_bf16 v[64:79], v[68:71], v[138:141], 0
	s_waitcnt lgkmcnt(1)
	v_mfma_f32_32x32x16_bf16 v[96:111], v[162:165], v[154:157], v[96:111]
	s_waitcnt lgkmcnt(0)
	v_mfma_f32_32x32x16_bf16 v[64:79], v[166:169], v[154:157], v[64:79]
	ds_read_b128 v[162:165], v219 offset:32768
	ds_read_b128 v[166:169], v219 offset:40960
	s_waitcnt lgkmcnt(1)
	v_mfma_f32_32x32x16_bf16 v[96:111], v[162:165], v[158:161], v[96:111]
	s_waitcnt lgkmcnt(0)
	v_mfma_f32_32x32x16_bf16 v[64:79], v[166:169], v[158:161], v[64:79]
	ds_read_b128 v[162:165], v220 offset:32768
	ds_read_b128 v[166:169], v220 offset:40960
	s_waitcnt lgkmcnt(1)
	v_mfma_f32_32x32x16_bf16 v[96:111], v[162:165], v[150:153], v[96:111]
	s_waitcnt lgkmcnt(0)
	v_mfma_f32_32x32x16_bf16 v[64:79], v[166:169], v[150:153], v[64:79]
	ds_read_b128 v[162:165], v221 offset:32768
	ds_read_b128 v[166:169], v221 offset:40960
	s_waitcnt lgkmcnt(1)
	v_mfma_f32_32x32x16_bf16 v[96:111], v[162:165], v[146:149], v[96:111]
	s_waitcnt lgkmcnt(0)
	v_mfma_f32_32x32x16_bf16 v[64:79], v[166:169], v[146:149], v[64:79]
	ds_read_b128 v[162:165], v222 offset:32768
	ds_read_b128 v[166:169], v222 offset:40960
	s_waitcnt lgkmcnt(1)
	v_mfma_f32_32x32x16_bf16 v[96:111], v[162:165], v[142:145], v[96:111]
	s_waitcnt lgkmcnt(0)
	v_mfma_f32_32x32x16_bf16 v[64:79], v[166:169], v[142:145], v[64:79]
	ds_read_b128 v[162:165], v224 offset:32768
	ds_read_b128 v[166:169], v224 offset:40960
	s_waitcnt lgkmcnt(1)
	v_mfma_f32_32x32x16_bf16 v[96:111], v[162:165], v[134:137], v[96:111]
	s_waitcnt lgkmcnt(0)
	v_mfma_f32_32x32x16_bf16 v[64:79], v[166:169], v[134:137], v[64:79]
	ds_read_b128 v[162:165], v223 offset:32768
	ds_read_b128 v[166:169], v223 offset:40960
	s_waitcnt lgkmcnt(1)
	v_mfma_f32_32x32x16_bf16 v[96:111], v[162:165], v[130:133], v[96:111]
	s_waitcnt lgkmcnt(0)
	v_mfma_f32_32x32x16_bf16 v[64:79], v[166:169], v[130:133], v[64:79]
.Lgqa_A_join:
	s_min_i32 s2, s39, s14
	s_mul_i32 s2, s2, s62
	s_lshl_b32 s72, s2, 6
	s_lshl_b64 s[2:3], s[72:73], 1
	s_add_u32 s12, s10, s2
	s_addc_u32 s13, s11, s3
	s_add_u32 s2, s8, s2
	s_addc_u32 s3, s9, s3
	global_load_dwordx4 v[162:165], v128, s[12:13]
	global_load_dwordx4 v[166:169], v198, s[12:13]
	global_load_dwordx4 v[170:173], v128, s[2:3]
	global_load_dwordx4 v[174:177], v198, s[2:3]
	ds_read_b64_tr_b16 v[80:81], v211 offset:0
	ds_read_b64_tr_b16 v[82:83], v211 offset:0x800
	ds_read_b64_tr_b16 v[84:85], v211 offset:0x1000
	ds_read_b64_tr_b16 v[86:87], v211 offset:0x1800
	ds_read_b64_tr_b16 v[88:89], v211 offset:0x2000
	ds_read_b64_tr_b16 v[90:91], v211 offset:0x2800
	ds_read_b64_tr_b16 v[92:93], v211 offset:0x3000
	ds_read_b64_tr_b16 v[94:95], v211 offset:0x3800
	s_waitcnt lgkmcnt(0)
	s_nop 0
	v_mfma_f32_32x32x16_bf16 v[0:15], v[80:83], v[124:127], v[0:15]
	v_mfma_f32_32x32x16_bf16 v[0:15], v[84:87], v[120:123], v[0:15]
	v_mfma_f32_32x32x16_bf16 v[0:15], v[88:91], v[112:115], v[0:15]
	ds_read_b64_tr_b16 v[80:81], v211 offset:0x200
	ds_read_b64_tr_b16 v[82:83], v211 offset:0xa00
	ds_read_b64_tr_b16 v[84:85], v211 offset:0x1200
	v_mfma_f32_32x32x16_bf16 v[0:15], v[92:95], v[116:119], v[0:15]
	ds_read_b64_tr_b16 v[86:87], v211 offset:0x1a00
	ds_read_b64_tr_b16 v[88:89], v211 offset:0x2200
	ds_read_b64_tr_b16 v[90:91], v211 offset:0x2a00
	ds_read_b64_tr_b16 v[92:93], v211 offset:0x3200
	ds_read_b64_tr_b16 v[94:95], v211 offset:0x3a00
	s_waitcnt lgkmcnt(0)
	v_mfma_f32_32x32x16_bf16 v[48:63], v[80:83], v[124:127], v[48:63]
	v_mfma_f32_32x32x16_bf16 v[48:63], v[84:87], v[120:123], v[48:63]
	v_mfma_f32_32x32x16_bf16 v[48:63], v[88:91], v[112:115], v[48:63]
	ds_read_b64_tr_b16 v[80:81], v211 offset:0x400
	ds_read_b64_tr_b16 v[82:83], v211 offset:0xc00
	ds_read_b64_tr_b16 v[84:85], v211 offset:0x1400
	ds_read_b64_tr_b16 v[86:87], v211 offset:0x1c00
	v_mfma_f32_32x32x16_bf16 v[48:63], v[92:95], v[116:119], v[48:63]
	ds_read_b64_tr_b16 v[88:89], v211 offset:0x2400
	ds_read_b64_tr_b16 v[90:91], v211 offset:0x2c00
	ds_read_b64_tr_b16 v[92:93], v211 offset:0x3400
	ds_read_b64_tr_b16 v[94:95], v211 offset:0x3c00
	s_waitcnt lgkmcnt(0)
	v_mfma_f32_32x32x16_bf16 v[32:47], v[80:83], v[124:127], v[32:47]
	v_exp_f32_e32 v80, v64
	v_exp_f32_e32 v81, v65
	v_exp_f32_e32 v64, v96
	v_exp_f32_e32 v65, v97
	v_exp_f32_e32 v82, v66
	v_exp_f32_e32 v83, v67
	v_exp_f32_e32 v66, v98
	v_exp_f32_e32 v67, v99
	v_mfma_f32_32x32x16_bf16 v[32:47], v[84:87], v[120:123], v[32:47]
	v_exp_f32_e32 v84, v68
	v_exp_f32_e32 v85, v69
	v_exp_f32_e32 v68, v100
	v_exp_f32_e32 v69, v101
	v_exp_f32_e32 v86, v70
	v_exp_f32_e32 v87, v71
	v_exp_f32_e32 v70, v102
	v_exp_f32_e32 v71, v103
	v_mfma_f32_32x32x16_bf16 v[32:47], v[88:91], v[112:115], v[32:47]
	v_exp_f32_e32 v194, v72
	v_exp_f32_e32 v195, v73
	ds_read_b64_tr_b16 v[72:73], v211 offset:0x600
	v_exp_f32_e32 v196, v74
	v_exp_f32_e32 v197, v75
	ds_read_b64_tr_b16 v[74:75], v211 offset:0xe00
	v_mfma_f32_32x32x16_bf16 v[32:47], v[92:95], v[116:119], v[32:47]
	v_exp_f32_e32 v92, v76
	v_exp_f32_e32 v93, v77
	ds_read_b64_tr_b16 v[76:77], v211 offset:0x1600
	v_exp_f32_e32 v94, v78
	v_exp_f32_e32 v95, v79
	ds_read_b64_tr_b16 v[78:79], v211 offset:0x1e00
	ds_read_b64_tr_b16 v[96:97], v211 offset:0x2600
	ds_read_b64_tr_b16 v[98:99], v211 offset:0x2e00
	ds_read_b64_tr_b16 v[100:101], v211 offset:0x3600
	ds_read_b64_tr_b16 v[102:103], v211 offset:0x3e00
	s_waitcnt lgkmcnt(0)
	v_mfma_f32_32x32x16_bf16 v[16:31], v[72:75], v[124:127], v[16:31]
	v_exp_f32_e32 v72, v104
	v_exp_f32_e32 v73, v105
	v_exp_f32_e32 v74, v106
	v_exp_f32_e32 v75, v107
	v_mfma_f32_32x32x16_bf16 v[16:31], v[76:79], v[120:123], v[16:31]
	v_exp_f32_e32 v76, v108
	v_exp_f32_e32 v77, v109
	v_exp_f32_e32 v78, v110
	v_exp_f32_e32 v79, v111
	s_barrier
	v_mfma_f32_32x32x16_bf16 v[16:31], v[96:99], v[112:115], v[16:31]
	s_waitcnt vmcnt(4)
	s_waitcnt vmcnt(7)
	ds_write_b128 v212, v[178:181] offset:16384
	s_waitcnt vmcnt(6)
	ds_write_b128 v213, v[182:185] offset:16384
	s_waitcnt vmcnt(5)
	ds_write_b128 v214, v[186:189] offset:49152
	s_waitcnt vmcnt(4)
	ds_write_b128 v215, v[190:193] offset:49152
	v_mfma_f32_32x32x16_bf16 v[16:31], v[100:103], v[116:119], v[16:31]
